# hooks: clamp +-7 then v_cvt_scalef32_pk_fp8_f32 with 2^-6 scale operand instead of mul 64 + clamp 448 + cvt_pk_fp8 (same fp8 e4m3 result, 32 fewer VALU per tile)
# speedup vs baseline: 1.0118x; 1.0118x over previous
; __device__ __forceinline__ bool conv_decode_moe(KA A, int t, ConvTile& c) {
;     unsigned char* ws = A->ws; c.f8 = 1; c.K = D; c.N = FFE; t -= 4096;
;     if (t < 14336) { const int hf = t / 7168, r2 = t % 7168, e = r2 / 896, r = r2 % 896, hk = r & 1, q = r >> 1; c.W = (hf ? A->in[I_MWU] : A->in[I_MWG]) + (size_t)e * D * FFE; c.WT = ws + WS_MUP + (size_t)e * 2 * FFE * D; c.k0 = 128 * (q / 28) + 64 * hk; c.n0 = 256 * (q % 28); c.kind = 2 + hf; return true; } t -= 14336;
;     if (t >= 7168) return false;
;     { const int e = t / 896, r = t % 896, hk = r & 1, q = r >> 1; c.W = A->in[I_MWD] + (size_t)e * FFE * D; c.WT = ws + WS_MDN + (size_t)e * D * FFE; c.K = FFE; c.N = D; c.k0 = 128 * (q >> 3) + 64 * hk; c.n0 = 256 * (q & 7); c.kind = 0; return true; }
; template <int NSLOT, bool MOE> __device__ __forceinline__ void conv_burst(const ConvHook& h, int bid, PG8_LAS unsigned char* T_, int tid) {
;     ...
;     const int p0 = (h.t0 >> 1) + bid, p1 = h.t1 >> 1;
.LBB0_805:
	s_mov_b32 s101, 0xc0e00000
	v_mov_b32_e32 v200, 0x40e00000
	v_mov_b32_e32 v201, 0x3c800000
	s_and_b32 s2, s73, 0x7ffffe00
	s_add_i32 s2, s28, s2
	s_addk_i32 s2, 0x100
	s_add_i32 s100, s2, 0x200
	s_cmp_lt_i32 s100, s60
	s_cselect_b32 s100, 1, 0
	s_cmp_lt_i32 s2, s60
	s_cselect_b64 s[68:69], -1, 0
	s_cmp_ge_i32 s2, s60
	s_cbranch_scc1 .LBB0_821
	s_lshl_b32 s12, s2, 1
	s_or_b32 s13, s12, 1
	s_cmpk_gt_i32 s13, 0x47ff
	s_waitcnt lgkmcnt(0)
	s_mov_b64 s[4:5], -1
	s_cbranch_scc0 .LBB0_809
	s_movk_i32 s24, 0x1c00
	s_mov_b64 s[4:5], 0
	s_cmpk_gt_u32 s12, 0x63ff
	s_mov_b64 s[6:7], 0
	s_cbranch_scc1 .LBB0_809
	s_add_i32 s13, s13, 0xb800
	s_bfe_u32 s6, s13, 0x90007
	s_mulk_i32 s6, 0x2493
	s_lshr_b32 s18, s6, 16
	s_load_dwordx2 s[6:7], s[14:15], 0xe0
	s_mul_i32 s19, s18, 0x380
	s_sub_i32 s13, s13, s19
	s_and_b32 s13, s13, 0xffff
	s_mul_hi_u32 s19, s18, 0x3800000
	s_mul_i32 s18, s18, 0x3800000
	s_waitcnt lgkmcnt(0)
	s_add_u32 s84, s6, s18
	s_addc_u32 s85, s7, s19
	s_lshl_b32 s6, s13, 3
	s_lshl_b32 s7, s13, 6
	s_and_b32 s6, s6, 0x1f80
	s_and_b32 s7, s7, 64
	s_or_b32 s65, s6, s7
	s_lshl_b32 s6, s13, 7
	s_and_b32 s42, s6, 0x700
	s_movk_i32 s24, 0x800
	s_mov_b64 s[6:7], -1

; #define GAS __attribute__((address_space(1)))
; #define LAS __attribute__((address_space(3)))
; #define LDS_BARRIER() do { asm volatile("s_waitcnt lgkmcnt(0)" ::: "memory"); __builtin_amdgcn_s_barrier(); asm volatile("" ::: "memory"); } while (0)
; __device__ __forceinline__ unsigned pk4_fp8(float a, float b, float c, float d) {
;     a = __builtin_amdgcn_fmed3f(a, -448.f, 448.f); b = __builtin_amdgcn_fmed3f(b, -448.f, 448.f); c = __builtin_amdgcn_fmed3f(c, -448.f, 448.f); d = __builtin_amdgcn_fmed3f(d, -448.f, 448.f);
;     int w = 0; w = __builtin_amdgcn_cvt_pk_fp8_f32(a, b, w, false); w = __builtin_amdgcn_cvt_pk_fp8_f32(c, d, w, true); return (unsigned)w; }
; template <class RowMap>
; __device__ __forceinline__ void conv_store_fp8(const f32x4 (&r)[8], unsigned char* WT, int Kbytes, int k0bytes, int n0, const RowMap rm, LAS unsigned char* T, int tid, int wave, int lane) {
;     const int s = 2 * (lane & 3);
; #pragma unroll
;     for (int j = 0; j < 4; ++j) { const unsigned lo = pk4_fp8(r[0][j] * W8_SCALE, r[1][j] * W8_SCALE, r[2][j] * W8_SCALE, r[3][j] * W8_SCALE), hi = pk4_fp8(r[4][j] * W8_SCALE, r[5][j] * W8_SCALE, r[6][j] * W8_SCALE, r[7][j] * W8_SCALE);
;         *(LAS unsigned long long*)(T + (4 * lane + j) * 64 + 8 * (wave ^ s)) = (unsigned long long)lo | ((unsigned long long)hi << 32); }
;     LDS_BARRIER();
;     const int c16 = tid & 3, rr = tid >> 2;
; #pragma unroll
;     for (int q = 0; q < 2; ++q) { const int row = rr + 128 * q; const v4u v = *(const LAS v4u*)(T + row * 64 + 16 * (c16 ^ ((row >> 2) & 3)));
;         const int dr = rm(n0 + row); if (dr >= 0) *(GAS v4u*)(WT + (unsigned)((((dr >> 8) * (Kbytes >> 7) + (k0bytes >> 7)) << 15) + ((dr & 255) << 7) + (k0bytes & 127) + 16 * c16)) = v; }
;     LDS_BARRIER();
; }
.Lhw_done_2:
	v_med3_f32 v131, v2, s101, v200
	v_med3_f32 v149, v6, s101, v200
	v_mov_b32_e32 v132, v130
	v_cvt_scalef32_pk_fp8_f32 v132, v131, v149, v201
	v_med3_f32 v133, v10, s101, v200
	v_med3_f32 v148, v14, s101, v200
	v_cvt_scalef32_pk_fp8_f32 v132, v133, v148, v201 op_sel:[0,0,0,1]
	v_med3_f32 v131, v18, s101, v200
	v_med3_f32 v165, v22, s101, v200
	v_mov_b32_e32 v133, v130
	v_cvt_scalef32_pk_fp8_f32 v133, v131, v165, v201
	v_med3_f32 v148, v30, s101, v200
	v_med3_f32 v149, v26, s101, v200
	v_cvt_scalef32_pk_fp8_f32 v133, v148, v149, v201 op_sel:[0,0,0,1]
	v_med3_f32 v131, v3, s101, v200
	v_med3_f32 v166, v7, s101, v200
	v_mov_b32_e32 v148, v130
	v_cvt_scalef32_pk_fp8_f32 v148, v131, v166, v201
	v_med3_f32 v149, v11, s101, v200
	v_med3_f32 v165, v15, s101, v200
	v_cvt_scalef32_pk_fp8_f32 v148, v149, v165, v201 op_sel:[0,0,0,1]
	v_med3_f32 v131, v19, s101, v200
	v_med3_f32 v167, v23, s101, v200
	v_mov_b32_e32 v149, v130
	v_cvt_scalef32_pk_fp8_f32 v149, v131, v167, v201
	v_med3_f32 v165, v31, s101, v200
	v_med3_f32 v166, v27, s101, v200
	v_cvt_scalef32_pk_fp8_f32 v149, v165, v166, v201 op_sel:[0,0,0,1]
	v_med3_f32 v131, v4, s101, v200
	s_cmp_lg_u32 s1, 0
	ds_write2_b64 v164, v[132:133], v[148:149] offset1:8
	v_med3_f32 v149, v8, s101, v200
	v_mov_b32_e32 v132, v130
	v_cvt_scalef32_pk_fp8_f32 v132, v131, v149, v201
	v_med3_f32 v133, v12, s101, v200
	v_med3_f32 v148, v16, s101, v200
	v_cvt_scalef32_pk_fp8_f32 v132, v133, v148, v201 op_sel:[0,0,0,1]
	v_med3_f32 v131, v20, s101, v200
	v_med3_f32 v165, v24, s101, v200
	v_mov_b32_e32 v133, v130
	v_cvt_scalef32_pk_fp8_f32 v133, v131, v165, v201
	v_med3_f32 v148, v32, s101, v200
	v_med3_f32 v149, v28, s101, v200
	v_cvt_scalef32_pk_fp8_f32 v133, v148, v149, v201 op_sel:[0,0,0,1]
	v_med3_f32 v131, v5, s101, v200
	v_med3_f32 v166, v9, s101, v200
	v_mov_b32_e32 v148, v130
	v_cvt_scalef32_pk_fp8_f32 v148, v131, v166, v201
	v_med3_f32 v149, v13, s101, v200
	v_med3_f32 v165, v17, s101, v200
	v_cvt_scalef32_pk_fp8_f32 v148, v149, v165, v201 op_sel:[0,0,0,1]
	v_med3_f32 v131, v21, s101, v200
	v_med3_f32 v167, v25, s101, v200
	v_mov_b32_e32 v149, v130
	v_cvt_scalef32_pk_fp8_f32 v149, v131, v167, v201
	v_med3_f32 v165, v33, s101, v200
	v_med3_f32 v166, v29, s101, v200
	v_cvt_scalef32_pk_fp8_f32 v149, v165, v166, v201 op_sel:[0,0,0,1]
	v_add_u32_e32 v131, s0, v156
	ds_write2_b64 v164, v[132:133], v[148:149] offset0:16 offset1:24
	s_cbranch_scc0 .LBB0_834
	s_lshl_b32 s6, s1, 7
	v_lshlrev_b32_e32 v148, 1, v131
	s_waitcnt lgkmcnt(0)
	s_barrier
	s_add_i32 s24, s6, 0xffffff00
	v_and_b32_e32 v133, 0x7f, v131
	v_and_b32_e32 v148, 0xffffff00, v148
	s_and_b32 s7, s64, 0x7f
	v_add_u32_e32 v148, s24, v148
	v_or_b32_e32 v133, s6, v133
	s_lshr_b32 s13, s64, 7
	v_add_u32_e32 v132, s7, v158
	v_cmp_lt_i32_e32 vcc, -1, v148
	v_lshlrev_b32_e32 v133, 7, v133
	s_and_saveexec_b64 s[6:7], vcc
	s_cbranch_execz .LBB0_831
	v_add_u32_e32 v149, v157, v159
	ds_read_b128 v[166:169], v149
	v_lshrrev_b32_e32 v148, 8, v148
	v_mul_u32_u24_e32 v148, s12, v148
	v_add_lshl_u32 v148, v148, s13, 15
	v_and_b32_e32 v149, 0x7f80, v133
	v_add3_u32 v148, v149, v132, v148
	s_waitcnt lgkmcnt(0)
	global_store_dwordx4 v148, v[166:169], s[40:41]

; #define GAS __attribute__((address_space(1)))
; #define LAS __attribute__((address_space(3)))
; #define LDS_BARRIER() do { asm volatile("s_waitcnt lgkmcnt(0)" ::: "memory"); __builtin_amdgcn_s_barrier(); asm volatile("" ::: "memory"); } while (0)
; __device__ __forceinline__ unsigned pk4_fp8(float a, float b, float c, float d) {
;     a = __builtin_amdgcn_fmed3f(a, -448.f, 448.f); b = __builtin_amdgcn_fmed3f(b, -448.f, 448.f); c = __builtin_amdgcn_fmed3f(c, -448.f, 448.f); d = __builtin_amdgcn_fmed3f(d, -448.f, 448.f);
;     int w = 0; w = __builtin_amdgcn_cvt_pk_fp8_f32(a, b, w, false); w = __builtin_amdgcn_cvt_pk_fp8_f32(c, d, w, true); return (unsigned)w; }
; template <class RowMap>
; __device__ __forceinline__ void conv_store_fp8(const f32x4 (&r)[8], unsigned char* WT, int Kbytes, int k0bytes, int n0, const RowMap rm, LAS unsigned char* T, int tid, int wave, int lane) {
;     const int s = 2 * (lane & 3);
; #pragma unroll
;     for (int j = 0; j < 4; ++j) { const unsigned lo = pk4_fp8(r[0][j] * W8_SCALE, r[1][j] * W8_SCALE, r[2][j] * W8_SCALE, r[3][j] * W8_SCALE), hi = pk4_fp8(r[4][j] * W8_SCALE, r[5][j] * W8_SCALE, r[6][j] * W8_SCALE, r[7][j] * W8_SCALE);
;         *(LAS unsigned long long*)(T + (4 * lane + j) * 64 + 8 * (wave ^ s)) = (unsigned long long)lo | ((unsigned long long)hi << 32); }
;     LDS_BARRIER();
;     const int c16 = tid & 3, rr = tid >> 2;
; #pragma unroll
;     for (int q = 0; q < 2; ++q) { const int row = rr + 128 * q; const v4u v = *(const LAS v4u*)(T + row * 64 + 16 * (c16 ^ ((row >> 2) & 3)));
;         const int dr = rm(n0 + row); if (dr >= 0) *(GAS v4u*)(WT + (unsigned)((((dr >> 8) * (Kbytes >> 7) + (k0bytes >> 7)) << 15) + ((dr & 255) << 7) + (k0bytes & 127) + 16 * c16)) = v; }
;     LDS_BARRIER();
; }
.Lhw_done_3:
	v_med3_f32 v131, v38, s101, v200
	v_med3_f32 v149, v42, s101, v200
	v_mov_b32_e32 v132, v130
	v_cvt_scalef32_pk_fp8_f32 v132, v131, v149, v201
	v_med3_f32 v133, v34, s101, v200
	v_med3_f32 v148, v46, s101, v200
	v_cvt_scalef32_pk_fp8_f32 v132, v133, v148, v201 op_sel:[0,0,0,1]
	v_med3_f32 v131, v50, s101, v200
	v_med3_f32 v165, v54, s101, v200
	v_mov_b32_e32 v133, v130
	v_cvt_scalef32_pk_fp8_f32 v133, v131, v165, v201
	v_med3_f32 v148, v62, s101, v200
	v_med3_f32 v149, v58, s101, v200
	v_cvt_scalef32_pk_fp8_f32 v133, v148, v149, v201 op_sel:[0,0,0,1]
	v_med3_f32 v131, v39, s101, v200
	v_med3_f32 v166, v43, s101, v200
	v_mov_b32_e32 v148, v130
	v_cvt_scalef32_pk_fp8_f32 v148, v131, v166, v201
	v_med3_f32 v149, v35, s101, v200
	v_med3_f32 v165, v47, s101, v200
	v_cvt_scalef32_pk_fp8_f32 v148, v149, v165, v201 op_sel:[0,0,0,1]
	v_med3_f32 v131, v51, s101, v200
	v_med3_f32 v167, v55, s101, v200
	v_mov_b32_e32 v149, v130
	v_cvt_scalef32_pk_fp8_f32 v149, v131, v167, v201
	v_med3_f32 v165, v63, s101, v200
	v_med3_f32 v166, v59, s101, v200
	v_cvt_scalef32_pk_fp8_f32 v149, v165, v166, v201 op_sel:[0,0,0,1]
	v_med3_f32 v131, v40, s101, v200
	s_cmp_lg_u32 s57, 0
	ds_write2_b64 v164, v[132:133], v[148:149] offset1:8
	v_med3_f32 v149, v44, s101, v200
	v_mov_b32_e32 v132, v130
	v_cvt_scalef32_pk_fp8_f32 v132, v131, v149, v201
	v_med3_f32 v133, v36, s101, v200
	v_med3_f32 v148, v48, s101, v200
	v_cvt_scalef32_pk_fp8_f32 v132, v133, v148, v201 op_sel:[0,0,0,1]
	v_med3_f32 v131, v52, s101, v200
	v_med3_f32 v165, v56, s101, v200
	v_mov_b32_e32 v133, v130
	v_cvt_scalef32_pk_fp8_f32 v133, v131, v165, v201
	v_med3_f32 v148, v64, s101, v200
	v_med3_f32 v149, v60, s101, v200
	v_cvt_scalef32_pk_fp8_f32 v133, v148, v149, v201 op_sel:[0,0,0,1]
	v_med3_f32 v131, v41, s101, v200
	v_med3_f32 v166, v45, s101, v200
	v_mov_b32_e32 v148, v130
	v_cvt_scalef32_pk_fp8_f32 v148, v131, v166, v201
	v_med3_f32 v149, v37, s101, v200
	v_med3_f32 v165, v49, s101, v200
	v_cvt_scalef32_pk_fp8_f32 v148, v149, v165, v201 op_sel:[0,0,0,1]
	v_med3_f32 v131, v53, s101, v200
	v_med3_f32 v167, v57, s101, v200
	v_mov_b32_e32 v149, v130
	v_cvt_scalef32_pk_fp8_f32 v149, v131, v167, v201
	v_med3_f32 v165, v65, s101, v200
	v_med3_f32 v166, v61, s101, v200
	v_cvt_scalef32_pk_fp8_f32 v149, v165, v166, v201 op_sel:[0,0,0,1]
	v_add_u32_e32 v131, s56, v156
	ds_write2_b64 v164, v[132:133], v[148:149] offset0:16 offset1:24
	s_cbranch_scc0 .LBB0_870
	s_lshl_b32 s6, s57, 7
	v_lshlrev_b32_e32 v148, 1, v131
	s_waitcnt lgkmcnt(0)
	s_barrier
	s_add_i32 s24, s6, 0xffffff00
	v_and_b32_e32 v133, 0x7f, v131
	v_and_b32_e32 v148, 0xffffff00, v148
	s_and_b32 s7, s58, 0x7f
	v_add_u32_e32 v148, s24, v148
	v_or_b32_e32 v133, s6, v133
	s_lshr_b32 s13, s58, 7
	v_add_u32_e32 v132, s7, v158
	v_cmp_lt_i32_e32 vcc, -1, v148
	v_lshlrev_b32_e32 v133, 7, v133
	s_and_saveexec_b64 s[6:7], vcc
	s_cbranch_execz .LBB0_867
	v_add_u32_e32 v149, v157, v159
	ds_read_b128 v[166:169], v149
	v_lshrrev_b32_e32 v148, 8, v148
	v_mul_u32_u24_e32 v148, s12, v148
	v_add_lshl_u32 v148, v148, s13, 15
	v_and_b32_e32 v149, 0x7f80, v133
	v_add3_u32 v148, v149, v132, v148
	s_waitcnt lgkmcnt(0)
	global_store_dwordx4 v148, v[166:169], s[86:87]

; #define GAS __attribute__((address_space(1)))
; #define LAS __attribute__((address_space(3)))
; #define LDS_BARRIER() do { asm volatile("s_waitcnt lgkmcnt(0)" ::: "memory"); __builtin_amdgcn_s_barrier(); asm volatile("" ::: "memory"); } while (0)
; __device__ __forceinline__ unsigned pk4_fp8(float a, float b, float c, float d) {
;     a = __builtin_amdgcn_fmed3f(a, -448.f, 448.f); b = __builtin_amdgcn_fmed3f(b, -448.f, 448.f); c = __builtin_amdgcn_fmed3f(c, -448.f, 448.f); d = __builtin_amdgcn_fmed3f(d, -448.f, 448.f);
;     int w = 0; w = __builtin_amdgcn_cvt_pk_fp8_f32(a, b, w, false); w = __builtin_amdgcn_cvt_pk_fp8_f32(c, d, w, true); return (unsigned)w; }
; template <class RowMap>
; __device__ __forceinline__ void conv_store_fp8(const f32x4 (&r)[8], unsigned char* WT, int Kbytes, int k0bytes, int n0, const RowMap rm, LAS unsigned char* T, int tid, int wave, int lane) {
;     const int s = 2 * (lane & 3);
; #pragma unroll
;     for (int j = 0; j < 4; ++j) { const unsigned lo = pk4_fp8(r[0][j] * W8_SCALE, r[1][j] * W8_SCALE, r[2][j] * W8_SCALE, r[3][j] * W8_SCALE), hi = pk4_fp8(r[4][j] * W8_SCALE, r[5][j] * W8_SCALE, r[6][j] * W8_SCALE, r[7][j] * W8_SCALE);
;         *(LAS unsigned long long*)(T + (4 * lane + j) * 64 + 8 * (wave ^ s)) = (unsigned long long)lo | ((unsigned long long)hi << 32); }
;     LDS_BARRIER();
;     const int c16 = tid & 3, rr = tid >> 2;
; #pragma unroll
;     for (int q = 0; q < 2; ++q) { const int row = rr + 128 * q; const v4u v = *(const LAS v4u*)(T + row * 64 + 16 * (c16 ^ ((row >> 2) & 3)));
;         const int dr = rm(n0 + row); if (dr >= 0) *(GAS v4u*)(WT + (unsigned)((((dr >> 8) * (Kbytes >> 7) + (k0bytes >> 7)) << 15) + ((dr & 255) << 7) + (k0bytes & 127) + 16 * c16)) = v; }
;     LDS_BARRIER();
; }
.Lhw_done_4:
	v_med3_f32 v131, v70, s101, v200
	v_med3_f32 v149, v74, s101, v200
	v_mov_b32_e32 v132, v130
	v_cvt_scalef32_pk_fp8_f32 v132, v131, v149, v201
	v_med3_f32 v133, v66, s101, v200
	v_med3_f32 v148, v78, s101, v200
	v_cvt_scalef32_pk_fp8_f32 v132, v133, v148, v201 op_sel:[0,0,0,1]
	v_med3_f32 v131, v82, s101, v200
	v_med3_f32 v165, v86, s101, v200
	v_mov_b32_e32 v133, v130
	v_cvt_scalef32_pk_fp8_f32 v133, v131, v165, v201
	v_med3_f32 v148, v94, s101, v200
	v_med3_f32 v149, v90, s101, v200
	v_cvt_scalef32_pk_fp8_f32 v133, v148, v149, v201 op_sel:[0,0,0,1]
	v_med3_f32 v131, v71, s101, v200
	v_med3_f32 v166, v75, s101, v200
	v_mov_b32_e32 v148, v130
	v_cvt_scalef32_pk_fp8_f32 v148, v131, v166, v201
	v_med3_f32 v149, v67, s101, v200
	v_med3_f32 v165, v79, s101, v200
	v_cvt_scalef32_pk_fp8_f32 v148, v149, v165, v201 op_sel:[0,0,0,1]
	v_med3_f32 v131, v83, s101, v200
	v_med3_f32 v167, v87, s101, v200
	v_mov_b32_e32 v149, v130
	v_cvt_scalef32_pk_fp8_f32 v149, v131, v167, v201
	v_med3_f32 v165, v95, s101, v200
	v_med3_f32 v166, v91, s101, v200
	v_cvt_scalef32_pk_fp8_f32 v149, v165, v166, v201 op_sel:[0,0,0,1]
	v_med3_f32 v131, v72, s101, v200
	s_cmp_lg_u32 s27, 0
	ds_write2_b64 v164, v[132:133], v[148:149] offset1:8
	v_med3_f32 v149, v76, s101, v200
	v_mov_b32_e32 v132, v130
	v_cvt_scalef32_pk_fp8_f32 v132, v131, v149, v201
	v_med3_f32 v133, v68, s101, v200
	v_med3_f32 v148, v80, s101, v200
	v_cvt_scalef32_pk_fp8_f32 v132, v133, v148, v201 op_sel:[0,0,0,1]
	v_med3_f32 v131, v84, s101, v200
	v_med3_f32 v165, v88, s101, v200
	v_mov_b32_e32 v133, v130
	v_cvt_scalef32_pk_fp8_f32 v133, v131, v165, v201
	v_med3_f32 v148, v96, s101, v200
	v_med3_f32 v149, v92, s101, v200
	v_cvt_scalef32_pk_fp8_f32 v133, v148, v149, v201 op_sel:[0,0,0,1]
	v_med3_f32 v131, v73, s101, v200
	v_med3_f32 v166, v77, s101, v200
	v_mov_b32_e32 v148, v130
	v_cvt_scalef32_pk_fp8_f32 v148, v131, v166, v201
	v_med3_f32 v149, v69, s101, v200
	v_med3_f32 v165, v81, s101, v200
	v_cvt_scalef32_pk_fp8_f32 v148, v149, v165, v201 op_sel:[0,0,0,1]
	v_med3_f32 v131, v85, s101, v200
	v_med3_f32 v167, v89, s101, v200
	v_mov_b32_e32 v149, v130
	v_cvt_scalef32_pk_fp8_f32 v149, v131, v167, v201
	v_med3_f32 v165, v97, s101, v200
	v_med3_f32 v166, v93, s101, v200
	v_cvt_scalef32_pk_fp8_f32 v149, v165, v166, v201 op_sel:[0,0,0,1]
	v_add_u32_e32 v131, s20, v156
	ds_write2_b64 v164, v[132:133], v[148:149] offset0:16 offset1:24
	s_cbranch_scc0 .LBB0_905
	s_lshl_b32 s6, s27, 7
	v_lshlrev_b32_e32 v148, 1, v131
	s_waitcnt lgkmcnt(0)
	s_barrier
	s_add_i32 s24, s6, 0xffffff00
	v_and_b32_e32 v133, 0x7f, v131
	v_and_b32_e32 v148, 0xffffff00, v148
	s_and_b32 s7, s29, 0x7f
	v_add_u32_e32 v148, s24, v148
	v_or_b32_e32 v133, s6, v133
	s_lshr_b32 s13, s29, 7
	v_add_u32_e32 v132, s7, v158
	v_cmp_lt_i32_e32 vcc, -1, v148
	v_lshlrev_b32_e32 v133, 7, v133
	s_and_saveexec_b64 s[6:7], vcc
	s_cbranch_execz .LBB0_902
	v_add_u32_e32 v149, v157, v159
	ds_read_b128 v[166:169], v149
	v_lshrrev_b32_e32 v148, 8, v148
	v_mul_u32_u24_e32 v148, s12, v148
	v_add_lshl_u32 v148, v148, s13, 15
	v_and_b32_e32 v149, 0x7f80, v133
	v_add3_u32 v148, v149, v132, v148
	s_waitcnt lgkmcnt(0)
	global_store_dwordx4 v148, v[166:169], s[90:91]

; #define GAS __attribute__((address_space(1)))
; #define LAS __attribute__((address_space(3)))
; #define LDS_BARRIER() do { asm volatile("s_waitcnt lgkmcnt(0)" ::: "memory"); __builtin_amdgcn_s_barrier(); asm volatile("" ::: "memory"); } while (0)
; __device__ __forceinline__ unsigned pk4_fp8(float a, float b, float c, float d) {
;     a = __builtin_amdgcn_fmed3f(a, -448.f, 448.f); b = __builtin_amdgcn_fmed3f(b, -448.f, 448.f); c = __builtin_amdgcn_fmed3f(c, -448.f, 448.f); d = __builtin_amdgcn_fmed3f(d, -448.f, 448.f);
;     int w = 0; w = __builtin_amdgcn_cvt_pk_fp8_f32(a, b, w, false); w = __builtin_amdgcn_cvt_pk_fp8_f32(c, d, w, true); return (unsigned)w; }
; template <class RowMap>
; __device__ __forceinline__ void conv_store_fp8(const f32x4 (&r)[8], unsigned char* WT, int Kbytes, int k0bytes, int n0, const RowMap rm, LAS unsigned char* T, int tid, int wave, int lane) {
;     const int s = 2 * (lane & 3);
; #pragma unroll
;     for (int j = 0; j < 4; ++j) { const unsigned lo = pk4_fp8(r[0][j] * W8_SCALE, r[1][j] * W8_SCALE, r[2][j] * W8_SCALE, r[3][j] * W8_SCALE), hi = pk4_fp8(r[4][j] * W8_SCALE, r[5][j] * W8_SCALE, r[6][j] * W8_SCALE, r[7][j] * W8_SCALE);
;         *(LAS unsigned long long*)(T + (4 * lane + j) * 64 + 8 * (wave ^ s)) = (unsigned long long)lo | ((unsigned long long)hi << 32); }
;     LDS_BARRIER();
;     const int c16 = tid & 3, rr = tid >> 2;
; #pragma unroll
;     for (int q = 0; q < 2; ++q) { const int row = rr + 128 * q; const v4u v = *(const LAS v4u*)(T + row * 64 + 16 * (c16 ^ ((row >> 2) & 3)));
;         const int dr = rm(n0 + row); if (dr >= 0) *(GAS v4u*)(WT + (unsigned)((((dr >> 8) * (Kbytes >> 7) + (k0bytes >> 7)) << 15) + ((dr & 255) << 7) + (k0bytes & 127) + 16 * c16)) = v; }
;     LDS_BARRIER();
; }
.Lhw_done_5:
	v_med3_f32 v131, v102, s101, v200
	v_med3_f32 v149, v106, s101, v200
	v_mov_b32_e32 v132, v130
	v_cvt_scalef32_pk_fp8_f32 v132, v131, v149, v201
	v_med3_f32 v133, v98, s101, v200
	v_med3_f32 v148, v110, s101, v200
	v_cvt_scalef32_pk_fp8_f32 v132, v133, v148, v201 op_sel:[0,0,0,1]
	v_med3_f32 v131, v114, s101, v200
	v_med3_f32 v165, v118, s101, v200
	v_mov_b32_e32 v133, v130
	v_cvt_scalef32_pk_fp8_f32 v133, v131, v165, v201
	v_med3_f32 v148, v126, s101, v200
	v_med3_f32 v149, v122, s101, v200
	v_cvt_scalef32_pk_fp8_f32 v133, v148, v149, v201 op_sel:[0,0,0,1]
	v_med3_f32 v131, v103, s101, v200
	v_med3_f32 v166, v107, s101, v200
	v_mov_b32_e32 v148, v130
	v_cvt_scalef32_pk_fp8_f32 v148, v131, v166, v201
	v_med3_f32 v149, v99, s101, v200
	v_med3_f32 v165, v111, s101, v200
	v_cvt_scalef32_pk_fp8_f32 v148, v149, v165, v201 op_sel:[0,0,0,1]
	v_med3_f32 v131, v115, s101, v200
	v_med3_f32 v167, v119, s101, v200
	v_mov_b32_e32 v149, v130
	v_cvt_scalef32_pk_fp8_f32 v149, v131, v167, v201
	v_med3_f32 v165, v127, s101, v200
	v_med3_f32 v166, v123, s101, v200
	v_cvt_scalef32_pk_fp8_f32 v149, v165, v166, v201 op_sel:[0,0,0,1]
	v_med3_f32 v131, v104, s101, v200
	s_cmp_lg_u32 s24, 0
	ds_write2_b64 v164, v[132:133], v[148:149] offset1:8
	v_med3_f32 v149, v108, s101, v200
	v_mov_b32_e32 v132, v130
	v_cvt_scalef32_pk_fp8_f32 v132, v131, v149, v201
	v_med3_f32 v133, v100, s101, v200
	v_med3_f32 v148, v112, s101, v200
	v_cvt_scalef32_pk_fp8_f32 v132, v133, v148, v201 op_sel:[0,0,0,1]
	v_med3_f32 v131, v116, s101, v200
	v_med3_f32 v165, v120, s101, v200
	v_mov_b32_e32 v133, v130
	v_cvt_scalef32_pk_fp8_f32 v133, v131, v165, v201
	v_med3_f32 v148, v128, s101, v200
	v_med3_f32 v149, v124, s101, v200
	v_cvt_scalef32_pk_fp8_f32 v133, v148, v149, v201 op_sel:[0,0,0,1]
	v_med3_f32 v131, v105, s101, v200
	v_med3_f32 v166, v109, s101, v200
	v_mov_b32_e32 v148, v130
	v_cvt_scalef32_pk_fp8_f32 v148, v131, v166, v201
	v_med3_f32 v149, v101, s101, v200
	v_med3_f32 v165, v113, s101, v200
	v_cvt_scalef32_pk_fp8_f32 v148, v149, v165, v201 op_sel:[0,0,0,1]
	v_med3_f32 v131, v117, s101, v200
	v_med3_f32 v167, v121, s101, v200
	v_mov_b32_e32 v149, v130
	v_cvt_scalef32_pk_fp8_f32 v149, v131, v167, v201
	v_med3_f32 v165, v129, s101, v200
	v_med3_f32 v166, v125, s101, v200
	v_cvt_scalef32_pk_fp8_f32 v149, v165, v166, v201 op_sel:[0,0,0,1]
	v_add_u32_e32 v131, s19, v156
	ds_write2_b64 v164, v[132:133], v[148:149] offset0:16 offset1:24
	s_cbranch_scc0 .LBB0_941
	s_waitcnt lgkmcnt(0)
	s_lshl_b32 s4, s24, 7
	v_lshlrev_b32_e32 v148, 1, v131
	s_waitcnt lgkmcnt(0)
	s_barrier
	s_add_i32 s7, s4, 0xffffff00
	v_and_b32_e32 v133, 0x7f, v131
	v_and_b32_e32 v148, 0xffffff00, v148
	s_and_b32 s5, s18, 0x7f
	v_add_u32_e32 v148, s7, v148
	v_or_b32_e32 v133, s4, v133
	s_lshr_b32 s6, s18, 7
	v_add_u32_e32 v132, s5, v158
	v_cmp_lt_i32_e32 vcc, -1, v148
	v_lshlrev_b32_e32 v133, 7, v133
	s_and_saveexec_b64 s[4:5], vcc
	s_cbranch_execz .LBB0_938
	v_add_u32_e32 v149, v157, v159
	ds_read_b128 v[166:169], v149
	v_lshrrev_b32_e32 v148, 8, v148
	v_mul_u32_u24_e32 v148, s2, v148
	v_add_lshl_u32 v148, v148, s6, 15
	v_and_b32_e32 v149, 0x7f80, v133
	v_add3_u32 v148, v149, v132, v148
	s_waitcnt lgkmcnt(0)
	global_store_dwordx4 v148, v[166:169], s[50:51]

; __device__ __forceinline__ bool conv_decode_moe(KA A, int t, ConvTile& c) {
;     unsigned char* ws = A->ws; c.f8 = 1; c.K = D; c.N = FFE; t -= 4096;
;     if (t < 14336) { const int hf = t / 7168, r2 = t % 7168, e = r2 / 896, r = r2 % 896, hk = r & 1, q = r >> 1; c.W = (hf ? A->in[I_MWU] : A->in[I_MWG]) + (size_t)e * D * FFE; c.WT = ws + WS_MUP + (size_t)e * 2 * FFE * D; c.k0 = 128 * (q / 28) + 64 * hk; c.n0 = 256 * (q % 28); c.kind = 2 + hf; return true; } t -= 14336;
;     if (t >= 7168) return false;
;     { const int e = t / 896, r = t % 896, hk = r & 1, q = r >> 1; c.W = A->in[I_MWD] + (size_t)e * FFE * D; c.WT = ws + WS_MDN + (size_t)e * D * FFE; c.K = FFE; c.N = D; c.k0 = 128 * (q >> 3) + 64 * hk; c.n0 = 256 * (q & 7); c.kind = 0; return true; }
; template <int NSLOT, bool MOE> __device__ __forceinline__ void conv_burst(const ConvHook& h, int bid, PG8_LAS unsigned char* T_, int tid) {
;     ...
;     const int p0 = (h.t0 >> 1) + bid, p1 = h.t1 >> 1;
.LBB0_2316:
	s_mov_b32 s101, 0xc0e00000
	v_mov_b32_e32 v200, 0x40e00000
	v_mov_b32_e32 v201, 0x3c800000
	s_and_b32 s2, s19, 0x7ffffe00
	s_add_i32 s2, s74, s2
	s_addk_i32 s2, 0x100
	s_add_i32 s100, s2, 0x200
	s_cmpk_lt_i32 s100, 0x2646
	s_cselect_b32 s100, 1, 0
	s_cmpk_lt_i32 s2, 0x2646
	s_cselect_b64 s[4:5], -1, 0
	s_cmpk_gt_i32 s2, 0x2645
	s_cbranch_scc1 .LBB0_2330
	s_lshl_b32 s18, s2, 1
	s_or_b32 s33, s18, 1
	s_cmpk_gt_i32 s33, 0x47ff
	s_mov_b64 s[12:13], -1
	s_cbranch_scc0 .LBB0_2319
	s_add_i32 s33, s33, 0xb800
	s_bfe_u32 s6, s33, 0x90007
	s_mulk_i32 s6, 0x2493
	s_lshr_b32 s12, s6, 16
	s_load_dwordx2 s[6:7], s[14:15], 0xe0
	s_mul_i32 s13, s12, 0x380
	s_sub_i32 s13, s33, s13
	s_and_b32 s13, s13, 0xffff
	s_mul_hi_u32 s24, s12, 0x3800000
	s_mul_i32 s12, s12, 0x3800000
	s_waitcnt lgkmcnt(0)
	s_add_u32 s6, s6, s12
	s_addc_u32 s7, s7, s24
	s_lshl_b32 s12, s13, 3
	s_lshl_b32 s24, s13, 6
	s_and_b32 s12, s12, 0x1f80
	s_and_b32 s24, s24, 64
	s_or_b32 s24, s12, s24
	s_lshl_b32 s12, s13, 7
	s_and_b32 s26, s12, 0x700
	s_mov_b64 s[12:13], 0

; #define GAS __attribute__((address_space(1)))
; #define LAS __attribute__((address_space(3)))
; #define LDS_BARRIER() do { asm volatile("s_waitcnt lgkmcnt(0)" ::: "memory"); __builtin_amdgcn_s_barrier(); asm volatile("" ::: "memory"); } while (0)
; __device__ __forceinline__ unsigned pk4_fp8(float a, float b, float c, float d) {
;     a = __builtin_amdgcn_fmed3f(a, -448.f, 448.f); b = __builtin_amdgcn_fmed3f(b, -448.f, 448.f); c = __builtin_amdgcn_fmed3f(c, -448.f, 448.f); d = __builtin_amdgcn_fmed3f(d, -448.f, 448.f);
;     int w = 0; w = __builtin_amdgcn_cvt_pk_fp8_f32(a, b, w, false); w = __builtin_amdgcn_cvt_pk_fp8_f32(c, d, w, true); return (unsigned)w; }
; template <class RowMap>
; __device__ __forceinline__ void conv_store_fp8(const f32x4 (&r)[8], unsigned char* WT, int Kbytes, int k0bytes, int n0, const RowMap rm, LAS unsigned char* T, int tid, int wave, int lane) {
;     const int s = 2 * (lane & 3);
; #pragma unroll
;     for (int j = 0; j < 4; ++j) { const unsigned lo = pk4_fp8(r[0][j] * W8_SCALE, r[1][j] * W8_SCALE, r[2][j] * W8_SCALE, r[3][j] * W8_SCALE), hi = pk4_fp8(r[4][j] * W8_SCALE, r[5][j] * W8_SCALE, r[6][j] * W8_SCALE, r[7][j] * W8_SCALE);
;         *(LAS unsigned long long*)(T + (4 * lane + j) * 64 + 8 * (wave ^ s)) = (unsigned long long)lo | ((unsigned long long)hi << 32); }
;     LDS_BARRIER();
;     const int c16 = tid & 3, rr = tid >> 2;
; #pragma unroll
;     for (int q = 0; q < 2; ++q) { const int row = rr + 128 * q; const v4u v = *(const LAS v4u*)(T + row * 64 + 16 * (c16 ^ ((row >> 2) & 3)));
;         const int dr = rm(n0 + row); if (dr >= 0) *(GAS v4u*)(WT + (unsigned)((((dr >> 8) * (Kbytes >> 7) + (k0bytes >> 7)) << 15) + ((dr & 255) << 7) + (k0bytes & 127) + 16 * c16)) = v; }
;     LDS_BARRIER();
; }
.Lhw_done_7:
	v_med3_f32 v131, v2, s101, v200
	v_med3_f32 v153, v6, s101, v200
	v_mov_b32_e32 v132, v130
	v_cvt_scalef32_pk_fp8_f32 v132, v131, v153, v201
	v_med3_f32 v133, v10, s101, v200
	v_med3_f32 v152, v14, s101, v200
	v_cvt_scalef32_pk_fp8_f32 v132, v133, v152, v201 op_sel:[0,0,0,1]
	v_med3_f32 v131, v18, s101, v200
	v_med3_f32 v158, v22, s101, v200
	v_mov_b32_e32 v133, v130
	v_cvt_scalef32_pk_fp8_f32 v133, v131, v158, v201
	v_med3_f32 v152, v50, s101, v200
	v_med3_f32 v153, v54, s101, v200
	v_cvt_scalef32_pk_fp8_f32 v133, v152, v153, v201 op_sel:[0,0,0,1]
	v_med3_f32 v131, v3, s101, v200
	v_med3_f32 v159, v7, s101, v200
	v_mov_b32_e32 v152, v130
	v_cvt_scalef32_pk_fp8_f32 v152, v131, v159, v201
	v_med3_f32 v153, v11, s101, v200
	v_med3_f32 v158, v15, s101, v200
	v_cvt_scalef32_pk_fp8_f32 v152, v153, v158, v201 op_sel:[0,0,0,1]
	v_med3_f32 v131, v19, s101, v200
	v_med3_f32 v172, v23, s101, v200
	v_mov_b32_e32 v153, v130
	v_cvt_scalef32_pk_fp8_f32 v153, v131, v172, v201
	v_med3_f32 v158, v51, s101, v200
	v_med3_f32 v159, v55, s101, v200
	v_cvt_scalef32_pk_fp8_f32 v153, v158, v159, v201 op_sel:[0,0,0,1]
	v_med3_f32 v131, v4, s101, v200
	s_cmp_lg_u32 s12, 0
	ds_write2_b64 v171, v[132:133], v[152:153] offset1:8
	v_med3_f32 v153, v8, s101, v200
	v_mov_b32_e32 v132, v130
	v_cvt_scalef32_pk_fp8_f32 v132, v131, v153, v201
	v_med3_f32 v133, v12, s101, v200
	v_med3_f32 v152, v16, s101, v200
	v_cvt_scalef32_pk_fp8_f32 v132, v133, v152, v201 op_sel:[0,0,0,1]
	v_med3_f32 v131, v20, s101, v200
	v_med3_f32 v158, v24, s101, v200
	v_mov_b32_e32 v133, v130
	v_cvt_scalef32_pk_fp8_f32 v133, v131, v158, v201
	v_med3_f32 v152, v52, s101, v200
	v_med3_f32 v153, v56, s101, v200
	v_cvt_scalef32_pk_fp8_f32 v133, v152, v153, v201 op_sel:[0,0,0,1]
	v_med3_f32 v131, v5, s101, v200
	v_med3_f32 v159, v9, s101, v200
	v_mov_b32_e32 v152, v130
	v_cvt_scalef32_pk_fp8_f32 v152, v131, v159, v201
	v_med3_f32 v153, v13, s101, v200
	v_med3_f32 v158, v17, s101, v200
	v_cvt_scalef32_pk_fp8_f32 v152, v153, v158, v201 op_sel:[0,0,0,1]
	v_med3_f32 v131, v21, s101, v200
	v_med3_f32 v172, v25, s101, v200
	v_mov_b32_e32 v153, v130
	v_cvt_scalef32_pk_fp8_f32 v153, v131, v172, v201
	v_med3_f32 v158, v53, s101, v200
	v_med3_f32 v159, v57, s101, v200
	v_cvt_scalef32_pk_fp8_f32 v153, v158, v159, v201 op_sel:[0,0,0,1]
	ds_write2_b64 v171, v[132:133], v[152:153] offset0:16 offset1:24
	s_cbranch_scc0 .LBB0_2350
	s_lshl_b32 s12, s12, 7
	v_add_lshl_u32 v132, s24, v160, 1
	s_waitcnt lgkmcnt(0)
	s_barrier
	s_add_i32 s47, s12, 0xffffff00
	v_and_b32_e32 v132, 0xffffff00, v132
	s_and_b32 s13, s33, 0x7f
	v_add_u32_e32 v133, s47, v132
	v_or_b32_e32 v132, s12, v166
	s_lshr_b32 s37, s33, 7
	v_add_u32_e32 v131, s13, v162
	v_cmp_lt_i32_e32 vcc, -1, v133
	v_lshlrev_b32_e32 v132, 7, v132
	s_and_saveexec_b64 s[12:13], vcc
	s_cbranch_execz .LBB0_2339
	v_add_u32_e32 v152, v161, v163
	ds_read_b128 v[172:175], v152
	v_lshrrev_b32_e32 v133, 8, v133
	v_mul_u32_u24_e32 v133, s26, v133
	v_add_lshl_u32 v133, v133, s37, 15
	v_and_b32_e32 v152, 0x7f80, v132
	v_add3_u32 v133, v152, v131, v133
	s_waitcnt lgkmcnt(0)
	global_store_dwordx4 v133, v[172:175], s[6:7]

; #define GAS __attribute__((address_space(1)))
; #define LAS __attribute__((address_space(3)))
; #define LDS_BARRIER() do { asm volatile("s_waitcnt lgkmcnt(0)" ::: "memory"); __builtin_amdgcn_s_barrier(); asm volatile("" ::: "memory"); } while (0)
; __device__ __forceinline__ unsigned pk4_fp8(float a, float b, float c, float d) {
;     a = __builtin_amdgcn_fmed3f(a, -448.f, 448.f); b = __builtin_amdgcn_fmed3f(b, -448.f, 448.f); c = __builtin_amdgcn_fmed3f(c, -448.f, 448.f); d = __builtin_amdgcn_fmed3f(d, -448.f, 448.f);
;     int w = 0; w = __builtin_amdgcn_cvt_pk_fp8_f32(a, b, w, false); w = __builtin_amdgcn_cvt_pk_fp8_f32(c, d, w, true); return (unsigned)w; }
; template <class RowMap>
; __device__ __forceinline__ void conv_store_fp8(const f32x4 (&r)[8], unsigned char* WT, int Kbytes, int k0bytes, int n0, const RowMap rm, LAS unsigned char* T, int tid, int wave, int lane) {
;     const int s = 2 * (lane & 3);
; #pragma unroll
;     for (int j = 0; j < 4; ++j) { const unsigned lo = pk4_fp8(r[0][j] * W8_SCALE, r[1][j] * W8_SCALE, r[2][j] * W8_SCALE, r[3][j] * W8_SCALE), hi = pk4_fp8(r[4][j] * W8_SCALE, r[5][j] * W8_SCALE, r[6][j] * W8_SCALE, r[7][j] * W8_SCALE);
;         *(LAS unsigned long long*)(T + (4 * lane + j) * 64 + 8 * (wave ^ s)) = (unsigned long long)lo | ((unsigned long long)hi << 32); }
;     LDS_BARRIER();
;     const int c16 = tid & 3, rr = tid >> 2;
; #pragma unroll
;     for (int q = 0; q < 2; ++q) { const int row = rr + 128 * q; const v4u v = *(const LAS v4u*)(T + row * 64 + 16 * (c16 ^ ((row >> 2) & 3)));
;         const int dr = rm(n0 + row); if (dr >= 0) *(GAS v4u*)(WT + (unsigned)((((dr >> 8) * (Kbytes >> 7) + (k0bytes >> 7)) << 15) + ((dr & 255) << 7) + (k0bytes & 127) + 16 * c16)) = v; }
;     LDS_BARRIER();
; }
.Lhw_done_8:
	v_med3_f32 v131, v26, s101, v200
	v_med3_f32 v153, v30, s101, v200
	v_mov_b32_e32 v132, v130
	v_cvt_scalef32_pk_fp8_f32 v132, v131, v153, v201
	v_med3_f32 v133, v34, s101, v200
	v_med3_f32 v152, v38, s101, v200
	v_cvt_scalef32_pk_fp8_f32 v132, v133, v152, v201 op_sel:[0,0,0,1]
	v_med3_f32 v131, v42, s101, v200
	v_med3_f32 v158, v46, s101, v200
	v_mov_b32_e32 v133, v130
	v_cvt_scalef32_pk_fp8_f32 v133, v131, v158, v201
	v_med3_f32 v152, v66, s101, v200
	v_med3_f32 v153, v70, s101, v200
	v_cvt_scalef32_pk_fp8_f32 v133, v152, v153, v201 op_sel:[0,0,0,1]
	v_med3_f32 v131, v27, s101, v200
	v_med3_f32 v159, v31, s101, v200
	v_mov_b32_e32 v152, v130
	v_cvt_scalef32_pk_fp8_f32 v152, v131, v159, v201
	v_med3_f32 v153, v35, s101, v200
	v_med3_f32 v158, v39, s101, v200
	v_cvt_scalef32_pk_fp8_f32 v152, v153, v158, v201 op_sel:[0,0,0,1]
	v_med3_f32 v131, v43, s101, v200
	v_med3_f32 v172, v47, s101, v200
	v_mov_b32_e32 v153, v130
	v_cvt_scalef32_pk_fp8_f32 v153, v131, v172, v201
	v_med3_f32 v158, v67, s101, v200
	v_med3_f32 v159, v71, s101, v200
	v_cvt_scalef32_pk_fp8_f32 v153, v158, v159, v201 op_sel:[0,0,0,1]
	v_med3_f32 v131, v28, s101, v200
	s_cmp_lg_u32 s12, 0
	ds_write2_b64 v171, v[132:133], v[152:153] offset1:8
	v_med3_f32 v153, v32, s101, v200
	v_mov_b32_e32 v132, v130
	v_cvt_scalef32_pk_fp8_f32 v132, v131, v153, v201
	v_med3_f32 v133, v36, s101, v200
	v_med3_f32 v152, v40, s101, v200
	v_cvt_scalef32_pk_fp8_f32 v132, v133, v152, v201 op_sel:[0,0,0,1]
	v_med3_f32 v131, v44, s101, v200
	v_med3_f32 v158, v48, s101, v200
	v_mov_b32_e32 v133, v130
	v_cvt_scalef32_pk_fp8_f32 v133, v131, v158, v201
	v_med3_f32 v152, v68, s101, v200
	v_med3_f32 v153, v72, s101, v200
	v_cvt_scalef32_pk_fp8_f32 v133, v152, v153, v201 op_sel:[0,0,0,1]
	v_med3_f32 v131, v29, s101, v200
	v_med3_f32 v159, v33, s101, v200
	v_mov_b32_e32 v152, v130
	v_cvt_scalef32_pk_fp8_f32 v152, v131, v159, v201
	v_med3_f32 v153, v37, s101, v200
	v_med3_f32 v158, v41, s101, v200
	v_cvt_scalef32_pk_fp8_f32 v152, v153, v158, v201 op_sel:[0,0,0,1]
	v_med3_f32 v131, v45, s101, v200
	v_med3_f32 v172, v49, s101, v200
	v_mov_b32_e32 v153, v130
	v_cvt_scalef32_pk_fp8_f32 v153, v131, v172, v201
	v_med3_f32 v158, v69, s101, v200
	v_med3_f32 v159, v73, s101, v200
	v_cvt_scalef32_pk_fp8_f32 v153, v158, v159, v201 op_sel:[0,0,0,1]
	ds_write2_b64 v171, v[132:133], v[152:153] offset0:16 offset1:24
	s_cbranch_scc0 .LBB0_2375
	s_lshl_b32 s12, s12, 7
	v_add_lshl_u32 v132, s24, v160, 1
	s_waitcnt lgkmcnt(0)
	s_barrier
	s_add_i32 s47, s12, 0xffffff00
	v_and_b32_e32 v132, 0xffffff00, v132
	s_and_b32 s13, s33, 0x7f
	v_add_u32_e32 v133, s47, v132
	v_or_b32_e32 v132, s12, v166
	s_lshr_b32 s37, s33, 7
	v_add_u32_e32 v131, s13, v162
	v_cmp_lt_i32_e32 vcc, -1, v133
	v_lshlrev_b32_e32 v132, 7, v132
	s_and_saveexec_b64 s[12:13], vcc
	s_cbranch_execz .LBB0_2372
	v_add_u32_e32 v152, v161, v163
	ds_read_b128 v[172:175], v152
	v_lshrrev_b32_e32 v133, 8, v133
	v_mul_u32_u24_e32 v133, s26, v133
	v_add_lshl_u32 v133, v133, s37, 15
	v_and_b32_e32 v152, 0x7f80, v132
	v_add3_u32 v133, v152, v131, v133
	s_waitcnt lgkmcnt(0)
	global_store_dwordx4 v133, v[172:175], s[6:7]

; #define GAS __attribute__((address_space(1)))
; #define LAS __attribute__((address_space(3)))
; #define LDS_BARRIER() do { asm volatile("s_waitcnt lgkmcnt(0)" ::: "memory"); __builtin_amdgcn_s_barrier(); asm volatile("" ::: "memory"); } while (0)
; __device__ __forceinline__ unsigned pk4_fp8(float a, float b, float c, float d) {
;     a = __builtin_amdgcn_fmed3f(a, -448.f, 448.f); b = __builtin_amdgcn_fmed3f(b, -448.f, 448.f); c = __builtin_amdgcn_fmed3f(c, -448.f, 448.f); d = __builtin_amdgcn_fmed3f(d, -448.f, 448.f);
;     int w = 0; w = __builtin_amdgcn_cvt_pk_fp8_f32(a, b, w, false); w = __builtin_amdgcn_cvt_pk_fp8_f32(c, d, w, true); return (unsigned)w; }
; template <class RowMap>
; __device__ __forceinline__ void conv_store_fp8(const f32x4 (&r)[8], unsigned char* WT, int Kbytes, int k0bytes, int n0, const RowMap rm, LAS unsigned char* T, int tid, int wave, int lane) {
;     const int s = 2 * (lane & 3);
; #pragma unroll
;     for (int j = 0; j < 4; ++j) { const unsigned lo = pk4_fp8(r[0][j] * W8_SCALE, r[1][j] * W8_SCALE, r[2][j] * W8_SCALE, r[3][j] * W8_SCALE), hi = pk4_fp8(r[4][j] * W8_SCALE, r[5][j] * W8_SCALE, r[6][j] * W8_SCALE, r[7][j] * W8_SCALE);
;         *(LAS unsigned long long*)(T + (4 * lane + j) * 64 + 8 * (wave ^ s)) = (unsigned long long)lo | ((unsigned long long)hi << 32); }
;     LDS_BARRIER();
;     const int c16 = tid & 3, rr = tid >> 2;
; #pragma unroll
;     for (int q = 0; q < 2; ++q) { const int row = rr + 128 * q; const v4u v = *(const LAS v4u*)(T + row * 64 + 16 * (c16 ^ ((row >> 2) & 3)));
;         const int dr = rm(n0 + row); if (dr >= 0) *(GAS v4u*)(WT + (unsigned)((((dr >> 8) * (Kbytes >> 7) + (k0bytes >> 7)) << 15) + ((dr & 255) << 7) + (k0bytes & 127) + 16 * c16)) = v; }
;     LDS_BARRIER();
; }
.Lhw_done_9:
	v_med3_f32 v131, v58, s101, v200
	v_med3_f32 v153, v62, s101, v200
	v_mov_b32_e32 v132, v130
	v_cvt_scalef32_pk_fp8_f32 v132, v131, v153, v201
	v_med3_f32 v133, v74, s101, v200
	v_med3_f32 v152, v78, s101, v200
	v_cvt_scalef32_pk_fp8_f32 v132, v133, v152, v201 op_sel:[0,0,0,1]
	v_med3_f32 v131, v82, s101, v200
	v_med3_f32 v158, v86, s101, v200
	v_mov_b32_e32 v133, v130
	v_cvt_scalef32_pk_fp8_f32 v133, v131, v158, v201
	v_med3_f32 v152, v102, s101, v200
	v_med3_f32 v153, v106, s101, v200
	v_cvt_scalef32_pk_fp8_f32 v133, v152, v153, v201 op_sel:[0,0,0,1]
	v_med3_f32 v131, v59, s101, v200
	v_med3_f32 v159, v63, s101, v200
	v_mov_b32_e32 v152, v130
	v_cvt_scalef32_pk_fp8_f32 v152, v131, v159, v201
	v_med3_f32 v153, v75, s101, v200
	v_med3_f32 v158, v79, s101, v200
	v_cvt_scalef32_pk_fp8_f32 v152, v153, v158, v201 op_sel:[0,0,0,1]
	v_med3_f32 v131, v83, s101, v200
	v_med3_f32 v172, v87, s101, v200
	v_mov_b32_e32 v153, v130
	v_cvt_scalef32_pk_fp8_f32 v153, v131, v172, v201
	v_med3_f32 v158, v103, s101, v200
	v_med3_f32 v159, v107, s101, v200
	v_cvt_scalef32_pk_fp8_f32 v153, v158, v159, v201 op_sel:[0,0,0,1]
	v_med3_f32 v131, v60, s101, v200
	s_cmp_lg_u32 s12, 0
	ds_write2_b64 v171, v[132:133], v[152:153] offset1:8
	v_med3_f32 v153, v64, s101, v200
	v_mov_b32_e32 v132, v130
	v_cvt_scalef32_pk_fp8_f32 v132, v131, v153, v201
	v_med3_f32 v133, v76, s101, v200
	v_med3_f32 v152, v80, s101, v200
	v_cvt_scalef32_pk_fp8_f32 v132, v133, v152, v201 op_sel:[0,0,0,1]
	v_med3_f32 v131, v84, s101, v200
	v_med3_f32 v158, v88, s101, v200
	v_mov_b32_e32 v133, v130
	v_cvt_scalef32_pk_fp8_f32 v133, v131, v158, v201
	v_med3_f32 v152, v104, s101, v200
	v_med3_f32 v153, v108, s101, v200
	v_cvt_scalef32_pk_fp8_f32 v133, v152, v153, v201 op_sel:[0,0,0,1]
	v_med3_f32 v131, v61, s101, v200
	v_med3_f32 v159, v65, s101, v200
	v_mov_b32_e32 v152, v130
	v_cvt_scalef32_pk_fp8_f32 v152, v131, v159, v201
	v_med3_f32 v153, v77, s101, v200
	v_med3_f32 v158, v81, s101, v200
	v_cvt_scalef32_pk_fp8_f32 v152, v153, v158, v201 op_sel:[0,0,0,1]
	v_med3_f32 v131, v85, s101, v200
	v_med3_f32 v172, v89, s101, v200
	v_mov_b32_e32 v153, v130
	v_cvt_scalef32_pk_fp8_f32 v153, v131, v172, v201
	v_med3_f32 v158, v105, s101, v200
	v_med3_f32 v159, v109, s101, v200
	v_cvt_scalef32_pk_fp8_f32 v153, v158, v159, v201 op_sel:[0,0,0,1]
	ds_write2_b64 v171, v[132:133], v[152:153] offset0:16 offset1:24
	s_cbranch_scc0 .LBB0_2407
	s_lshl_b32 s12, s12, 7
	v_add_lshl_u32 v132, s24, v160, 1
	s_waitcnt lgkmcnt(0)
	s_barrier
	s_add_i32 s47, s12, 0xffffff00
	v_and_b32_e32 v132, 0xffffff00, v132
	s_and_b32 s13, s33, 0x7f
	v_add_u32_e32 v133, s47, v132
	v_or_b32_e32 v132, s12, v166
	s_lshr_b32 s37, s33, 7
	v_add_u32_e32 v131, s13, v162
	v_cmp_lt_i32_e32 vcc, -1, v133
	v_lshlrev_b32_e32 v132, 7, v132
	s_and_saveexec_b64 s[12:13], vcc
	s_cbranch_execz .LBB0_2404
	v_add_u32_e32 v152, v161, v163
	ds_read_b128 v[172:175], v152
	v_lshrrev_b32_e32 v133, 8, v133
	v_mul_u32_u24_e32 v133, s26, v133
	v_add_lshl_u32 v133, v133, s37, 15
	v_and_b32_e32 v152, 0x7f80, v132
	v_add3_u32 v133, v152, v131, v133
	s_waitcnt lgkmcnt(0)
	global_store_dwordx4 v133, v[172:175], s[6:7]

; #define GAS __attribute__((address_space(1)))
; #define LAS __attribute__((address_space(3)))
; #define LDS_BARRIER() do { asm volatile("s_waitcnt lgkmcnt(0)" ::: "memory"); __builtin_amdgcn_s_barrier(); asm volatile("" ::: "memory"); } while (0)
; __device__ __forceinline__ unsigned pk4_fp8(float a, float b, float c, float d) {
;     a = __builtin_amdgcn_fmed3f(a, -448.f, 448.f); b = __builtin_amdgcn_fmed3f(b, -448.f, 448.f); c = __builtin_amdgcn_fmed3f(c, -448.f, 448.f); d = __builtin_amdgcn_fmed3f(d, -448.f, 448.f);
;     int w = 0; w = __builtin_amdgcn_cvt_pk_fp8_f32(a, b, w, false); w = __builtin_amdgcn_cvt_pk_fp8_f32(c, d, w, true); return (unsigned)w; }
; template <class RowMap>
; __device__ __forceinline__ void conv_store_fp8(const f32x4 (&r)[8], unsigned char* WT, int Kbytes, int k0bytes, int n0, const RowMap rm, LAS unsigned char* T, int tid, int wave, int lane) {
;     const int s = 2 * (lane & 3);
; #pragma unroll
;     for (int j = 0; j < 4; ++j) { const unsigned lo = pk4_fp8(r[0][j] * W8_SCALE, r[1][j] * W8_SCALE, r[2][j] * W8_SCALE, r[3][j] * W8_SCALE), hi = pk4_fp8(r[4][j] * W8_SCALE, r[5][j] * W8_SCALE, r[6][j] * W8_SCALE, r[7][j] * W8_SCALE);
;         *(LAS unsigned long long*)(T + (4 * lane + j) * 64 + 8 * (wave ^ s)) = (unsigned long long)lo | ((unsigned long long)hi << 32); }
;     LDS_BARRIER();
;     const int c16 = tid & 3, rr = tid >> 2;
; #pragma unroll
;     for (int q = 0; q < 2; ++q) { const int row = rr + 128 * q; const v4u v = *(const LAS v4u*)(T + row * 64 + 16 * (c16 ^ ((row >> 2) & 3)));
;         const int dr = rm(n0 + row); if (dr >= 0) *(GAS v4u*)(WT + (unsigned)((((dr >> 8) * (Kbytes >> 7) + (k0bytes >> 7)) << 15) + ((dr & 255) << 7) + (k0bytes & 127) + 16 * c16)) = v; }
;     LDS_BARRIER();
; }
.Lhw_done_10:
	v_med3_f32 v131, v94, s101, v200
	v_med3_f32 v153, v98, s101, v200
	v_mov_b32_e32 v132, v130
	v_cvt_scalef32_pk_fp8_f32 v132, v131, v153, v201
	v_med3_f32 v133, v90, s101, v200
	v_med3_f32 v152, v110, s101, v200
	v_cvt_scalef32_pk_fp8_f32 v132, v133, v152, v201 op_sel:[0,0,0,1]
	v_med3_f32 v131, v114, s101, v200
	v_med3_f32 v158, v118, s101, v200
	v_mov_b32_e32 v133, v130
	v_cvt_scalef32_pk_fp8_f32 v133, v131, v158, v201
	v_med3_f32 v152, v126, s101, v200
	v_med3_f32 v153, v122, s101, v200
	v_cvt_scalef32_pk_fp8_f32 v133, v152, v153, v201 op_sel:[0,0,0,1]
	v_med3_f32 v131, v95, s101, v200
	v_med3_f32 v159, v99, s101, v200
	v_mov_b32_e32 v152, v130
	v_cvt_scalef32_pk_fp8_f32 v152, v131, v159, v201
	v_med3_f32 v153, v91, s101, v200
	v_med3_f32 v158, v111, s101, v200
	v_cvt_scalef32_pk_fp8_f32 v152, v153, v158, v201 op_sel:[0,0,0,1]
	v_med3_f32 v131, v115, s101, v200
	v_med3_f32 v172, v119, s101, v200
	v_mov_b32_e32 v153, v130
	v_cvt_scalef32_pk_fp8_f32 v153, v131, v172, v201
	v_med3_f32 v158, v127, s101, v200
	v_med3_f32 v159, v123, s101, v200
	v_cvt_scalef32_pk_fp8_f32 v153, v158, v159, v201 op_sel:[0,0,0,1]
	v_med3_f32 v131, v96, s101, v200
	s_cmp_lg_u32 s6, 0
	ds_write2_b64 v171, v[132:133], v[152:153] offset1:8
	v_med3_f32 v153, v100, s101, v200
	v_mov_b32_e32 v132, v130
	v_cvt_scalef32_pk_fp8_f32 v132, v131, v153, v201
	v_med3_f32 v133, v92, s101, v200
	v_med3_f32 v152, v112, s101, v200
	v_cvt_scalef32_pk_fp8_f32 v132, v133, v152, v201 op_sel:[0,0,0,1]
	v_med3_f32 v131, v116, s101, v200
	v_med3_f32 v158, v120, s101, v200
	v_mov_b32_e32 v133, v130
	v_cvt_scalef32_pk_fp8_f32 v133, v131, v158, v201
	v_med3_f32 v152, v128, s101, v200
	v_med3_f32 v153, v124, s101, v200
	v_cvt_scalef32_pk_fp8_f32 v133, v152, v153, v201 op_sel:[0,0,0,1]
	v_med3_f32 v131, v97, s101, v200
	v_med3_f32 v159, v101, s101, v200
	v_mov_b32_e32 v152, v130
	v_cvt_scalef32_pk_fp8_f32 v152, v131, v159, v201
	v_med3_f32 v153, v93, s101, v200
	v_med3_f32 v158, v113, s101, v200
	v_cvt_scalef32_pk_fp8_f32 v152, v153, v158, v201 op_sel:[0,0,0,1]
	v_med3_f32 v131, v117, s101, v200
	v_med3_f32 v172, v121, s101, v200
	v_mov_b32_e32 v153, v130
	v_cvt_scalef32_pk_fp8_f32 v153, v131, v172, v201
	v_med3_f32 v158, v129, s101, v200
	v_med3_f32 v159, v125, s101, v200
	v_cvt_scalef32_pk_fp8_f32 v153, v158, v159, v201 op_sel:[0,0,0,1]
	ds_write2_b64 v171, v[132:133], v[152:153] offset0:16 offset1:24
	s_cbranch_scc0 .LBB0_2439
	s_lshl_b32 s6, s6, 7
	v_add_lshl_u32 v132, s2, v160, 1
	s_waitcnt lgkmcnt(0)
	s_barrier
	s_add_i32 s24, s6, 0xffffff00
	v_and_b32_e32 v132, 0xffffff00, v132
	s_and_b32 s7, s13, 0x7f
	v_add_u32_e32 v133, s24, v132
	v_or_b32_e32 v132, s6, v166
	s_lshr_b32 s18, s13, 7
	v_add_u32_e32 v131, s7, v162
	v_cmp_lt_i32_e32 vcc, -1, v133
	v_lshlrev_b32_e32 v132, 7, v132
	s_and_saveexec_b64 s[6:7], vcc
	s_cbranch_execz .LBB0_2436
	v_add_u32_e32 v152, v161, v163
	ds_read_b128 v[172:175], v152
	v_lshrrev_b32_e32 v133, 8, v133
	v_mul_u32_u24_e32 v133, s12, v133
	v_add_lshl_u32 v133, v133, s18, 15
	v_and_b32_e32 v152, 0x7f80, v132
	v_add3_u32 v133, v152, v131, v133
	s_waitcnt lgkmcnt(0)
	global_store_dwordx4 v133, v[172:175], s[4:5]
